# baseline (speedup 1.0000x reference)
.LBB1_26:
	s_waitcnt vmcnt(35)
	v_and_b32_e32 v113, 3, v0
	s_and_b32 s18, s2, 15
	v_cmp_eq_u32_e32 vcc, 0, v113
	v_cmp_gt_u32_e64 s[4:5], 12, v92
	s_and_b64 s[12:13], vcc, s[4:5]
	s_lshl_b32 s4, s3, 12
	s_lshl_b32 s5, s18, 8
	s_or_b32 s4, s4, s5
	s_mul_hi_i32 s5, s4, 0x6000
	s_mulk_i32 s4, 0x6000
	s_lshl_b32 s3, s3, 8
	s_add_u32 s16, s24, s4
	s_addc_u32 s17, s25, s5
	s_ashr_i32 s4, s21, 31
	s_lshr_b32 s4, s4, 29
	s_add_i32 s4, s21, s4
	s_ashr_i32 s19, s4, 3
	v_and_b32_e32 v101, 1, v74
	v_lshl_or_b32 v74, v91, 1, v95
	s_min_i32 s4, s19, 0xff
	v_mul_u32_u24_e32 v74, 0x60, v74
	v_lshlrev_b32_e32 v75, 1, v92
	s_mul_hi_i32 s5, s4, 0x6000
	s_mulk_i32 s4, 0x6000
	v_or3_b32 v88, v74, v75, v101
	s_add_u32 s4, s16, s4
	s_addc_u32 s5, s17, s5
	v_lshlrev_b64 v[102:103], 4, v[88:89]
	v_lshl_add_u64 v[104:105], s[4:5], 0, v[102:103]
	global_load_dwordx4 v[82:85], v[104:105], off
	global_load_dwordx4 v[74:77], v[104:105], off offset:512
	global_load_dwordx4 v[78:81], v[104:105], off offset:1024
	s_waitcnt vmcnt(5)
	v_mul_f32_e32 v88, 0xbfb8aa3b, v97
	v_mul_f32_e32 v99, 0x3c91a2b4, v88
	s_waitcnt vmcnt(4)
	v_mul_f32_e32 v88, 0x4038aa3b, v96
	v_mul_f32_e32 v104, 0x3c91a2b4, v88
	v_lshrrev_b32_e32 v88, 2, v92
	v_and_b32_e32 v92, 4, v92
	v_cmp_lt_u32_e64 s[4:5], 1, v93
	v_mov_b32_e32 v93, 0xd0
	v_cmp_ne_u32_e32 vcc, 0, v92
	v_lshlrev_b32_e32 v107, 3, v88
	v_sub_u32_e32 v88, 0, v107
	v_cndmask_b32_e32 v92, 0, v93, vcc
	v_add_u32_e32 v106, v92, v86
	v_and_b32_e32 v92, 12, v0
	v_mul_u32_u24_e32 v86, 0xd0, v101
	v_mad_u32_u24 v91, v91, 24, v92
	v_mul_u32_u24_e32 v93, 12, v95
	v_lshlrev_b32_e32 v92, 20, v101
	v_add3_u32 v112, v91, v86, v93
	v_lshl_or_b32 v86, s18, 21, v90
	v_add3_u32 v86, v86, s3, v92
	v_mul_f32_e32 v1, 0xbfb8aa3b, v1
	v_and_b32_e32 v114, 24, v88
	v_or_b32_e32 v88, v86, v94
	s_min_i32 s3, s19, 0xfe
	v_mul_f32_e32 v1, 0x3c91a2b4, v1
	s_waitcnt vmcnt(3)
	v_mul_f32_e32 v105, 0x4038aa3b, v100
	v_add_u32_e32 v108, 16, v106
	v_add_u32_e32 v109, 0x70, v106
	v_add_u32_e32 v110, 0x1b0, v106
	v_add_u32_e32 v111, 0x210, v106
	v_mul_u32_u24_e32 v113, 6, v113
	s_add_i32 s19, s3, 1
	v_lshl_add_u64 v[100:101], s[16:17], 0, v[102:103]
	v_lshl_add_u64 v[102:103], v[88:89], 1, s[14:15]
	s_sub_i32 s3, 0x7ff, s21
	v_mov_b32_e32 v115, 0x7f7f7f7f
	s_mov_b32 s16, 0x42700000
	s_mov_b32 s17, 0x41f00000
	s_mov_b32 s18, 0x41700000
	v_mov_b32_e32 v116, 0x6000
	v_mov_b32_e32 v117, 0x4b400000
	v_mov_b32_e32 v118, 0x4b400008
	v_mov_b32_e32 v119, 0x4b400010
	v_mbcnt_lo_u32_b32 v200, -1, 0
	v_mbcnt_hi_u32_b32 v200, -1, v200
	v_and_b32_e32 v201, 3, v200
	v_and_b32_e32 v202, 15, v200
	v_cmp_gt_u32_e32 vcc, 8, v202
	s_nop 1
	v_cndmask_b32_e64 v178, 0, v115, vcc
	v_cndmask_b32_e64 v179, v115, 0, vcc
	v_lshlrev_b32_e32 v181, 1, v201
	v_sub_u32_e32 v202, 22, v181
	v_lshlrev_b32_e64 v180, v202, 1
	v_sub_u32_e32 v202, 16, v181
	v_lshlrev_b32_e64 v181, v202, 1
	v_readfirstlane_b32 s51, v112
	v_lshrrev_b32_e32 v202, 4, v200
	v_lshlrev_b32_e32 v192, 5, v202
	v_bfe_u32 v202, v200, 2, 1
	v_mul_u32_u24_e32 v202, 0x110, v202
	v_add_u32_e32 v192, v192, v202
	s_mul_i32 s46, s51, 0xaaab
	s_lshr_b32 s46, s46, 15
	v_bfe_u32 v202, v200, 4, 1
	v_mul_u32_u24_e32 v184, 0x110, v202
	v_lshrrev_b32_e32 v202, 5, v200
	v_mul_u32_u24_e32 v202, 12, v202
	v_add_u32_e32 v184, v184, v202
	v_bfe_u32 v202, v200, 2, 2
	v_mul_u32_u24_e32 v164, 3, v202
	v_add3_u32 v184, v184, v164, v201
	v_add_u32_e32 v184, s46, v184
	v_add_u32_e32 v202, 0x100, v202
	v_lshrrev_b32_e32 v164, 4, v200
	v_and_b32_e32 v165, 1, v164
	v_mul_u32_u24_e32 v165, 0x110, v165
	v_lshrrev_b32_e32 v164, 1, v164
	v_lshl_add_u32 v165, v164, 2, v165
	v_add_u32_e32 v202, v202, v165
	v_cmp_eq_u32_e32 vcc, 3, v201
	s_nop 1
	v_cndmask_b32_e32 v184, v184, v202, vcc
	v_subrev_u32_e32 v185, s14, v102
	s_mov_b32 s44, s21
	s_mov_b32 s45, s22
	s_lshr_b32 s46, s44, 3
	s_add_i32 s46, s46, 1
	s_mul_i32 s46, s46, 0x6000
	s_mov_b32 s47, 0
	v_lshl_add_u64 v[196:197], v[100:101], 0, s[46:47]
	s_mov_b32 s42, 0x6000
	s_mov_b32 s43, 0
	s_sub_i32 s46, s44, 1
	s_sub_i32 s47, 0x800, s44
	s_and_b64 s[40:41], s[6:7], exec
	s_cselect_b32 s46, s46, s47
	s_cselect_b32 s41, 0, -1
	s_xor_b32 s40, s41, 0x400
	s_sub_i32 s40, s40, s41
	s_ashr_i32 s47, s46, 31
	s_lshl_b64 s[46:47], s[46:47], 10
	s_add_u32 s48, s14, s46
	s_addc_u32 s49, s15, s47
	s_waitcnt vmcnt(0) lgkmcnt(0)
	v_mov_b32_e32 v176, v87
	v_add_f32_e32 v169, -1.0, v87
	v_rcp_f32_e32 v186, v104
	s_nop 1
	v_mul_f32_e32 v188, v105, v186
	v_mov_b32_e32 v189, 0
	v_mov_b32_e32 v190, 0
	v_mov_b32_e32 v191, 0
	s_nop 1
	s_cmp_lt_i32 s44, s45
	s_cbranch_scc0 .Lscan_exit_st
	ds_read_b128 v[122:125], v192
	ds_read_b64 v[126:127], v192 offset:16
	s_waitcnt lgkmcnt(0)
	s_cmp_lt_u32 s51, 96
	s_cbranch_scc0 .Lscan_entry_b_st
	s_branch .Lscan_enter_a_st
	.p2align 8

.Lscan_entry_b_st:
	s_branch .Lscan_enter_b_st
	.p2align 8

.LBB2_12:
	s_or_b64 exec, exec, s[0:1]
	v_and_b32_e32 v97, 1, v74
	v_mov_b32_e32 v74, s8
	v_mov_b32_e32 v75, s9
	v_lshl_or_b32 v76, s2, 9, v0
	v_mov_b32_e32 v77, v87
	v_lshl_add_u64 v[74:75], v[76:77], 2, v[74:75]
	s_waitcnt lgkmcnt(0)
	s_barrier
	global_load_dword v118, v[74:75], off
	v_and_b32_e32 v74, 4, v90
	v_mov_b32_e32 v75, 0xd0
	v_cmp_ne_u32_e32 vcc, 0, v74
	v_and_b32_e32 v110, 3, v0
	v_cmp_gt_u32_e64 s[0:1], 12, v90
	v_cndmask_b32_e32 v74, 0, v75, vcc
	v_cmp_eq_u32_e32 vcc, 0, v110
	s_and_b64 s[4:5], vcc, s[0:1]
	s_lshl_b32 s1, s2, 21
	v_add_u32_e32 v109, v74, v86
	s_mul_i32 s0, s2, 0x600000
	v_lshl_or_b32 v74, v89, 1, v88
	s_and_b32 s2, s1, 0x1e00000
	v_mul_u32_u24_e32 v74, 0x60, v74
	v_lshlrev_b32_e32 v75, 1, v90
	s_add_u32 s0, s14, s0
	s_addc_u32 s1, s15, 0
	v_or3_b32 v86, v74, v75, v97
	v_lshl_add_u64 v[98:99], v[86:87], 4, s[0:1]
	s_mov_b64 s[0:1], 0x5a0000
	v_lshl_add_u64 v[100:101], v[98:99], 0, s[0:1]
	s_mov_b32 s0, 0x5a0000
	v_add_co_u32_e32 v102, vcc, s0, v98
	s_waitcnt vmcnt(4)
	v_mul_f32_e32 v86, 0xbfb8aa3b, v95
	v_addc_co_u32_e32 v103, vcc, 0, v99, vcc
	global_load_dwordx4 v[82:85], v[102:103], off
	global_load_dwordx4 v[74:77], v[100:101], off offset:512
	global_load_dwordx4 v[78:81], v[100:101], off offset:1024
	v_mul_f32_e32 v100, 0x3c91a2b4, v86
	s_waitcnt vmcnt(6)
	v_mul_f32_e32 v86, 0xbfb8aa3b, v94
	v_mul_f32_e32 v101, 0x3c91a2b4, v86
	s_waitcnt vmcnt(5)
	v_mul_f32_e32 v86, 0x4038aa3b, v93
	v_and_b32_e32 v0, 12, v0
	v_mul_f32_e32 v102, 0x3c91a2b4, v86
	v_lshrrev_b32_e32 v86, 2, v90
	v_mul_u32_u24_e32 v90, 0xd0, v97
	v_mad_u32_u24 v0, v89, 24, v0
	v_mul_u32_u24_e32 v88, 12, v88
	v_add3_u32 v93, v0, v90, v88
	v_or_b32_e32 v0, s2, v1
	v_lshlrev_b32_e32 v104, 3, v86
	v_lshlrev_b32_e32 v89, 20, v97
	v_lshl_add_u32 v0, s22, 8, v0
	v_sub_u32_e32 v86, 0, v104
	v_or3_b32 v0, v0, v89, v92
	v_and_b32_e32 v111, 24, v86
	v_lshlrev_b32_e32 v86, 1, v0
	s_mov_b64 s[6:7], 0x5a6000
	v_lshl_add_u64 v[0:1], s[12:13], 0, v[86:87]
	v_lshl_add_u64 v[86:87], v[98:99], 0, s[6:7]
	s_mov_b64 s[6:7], 0x5a6200
	v_lshl_add_u64 v[88:89], v[98:99], 0, s[6:7]
	s_mov_b64 s[6:7], 0x5a6400
	v_cmp_lt_u32_e64 s[0:1], 1, v91
	s_waitcnt vmcnt(4)
	v_mul_f32_e32 v103, 0x4038aa3b, v96
	s_mov_b32 s3, 0
	v_or_b32_e32 v105, 0x1c400, v109
	v_add_u32_e32 v106, 0x1c410, v109
	v_add_u32_e32 v107, 0x1c470, v109
	v_add_u32_e32 v108, 0x1c5b0, v109
	v_add_u32_e32 v109, 0x1c610, v109
	v_mul_u32_u24_e32 v110, 6, v110
	v_lshl_add_u64 v[90:91], v[98:99], 0, s[6:7]
	s_movk_i32 s22, 0x780
	s_movk_i32 s14, 0x7f
	s_movk_i32 s15, 0xf0
	v_mov_b32_e32 v112, 0x7f7f7f7f
	s_mov_b32 s17, 0x42700000
	s_mov_b32 s18, 0x41f00000
	s_mov_b32 s19, 0x41700000
	s_mov_b64 s[6:7], 0x12000
	s_mov_b64 s[8:9], 0x12200
	s_mov_b64 s[10:11], 0x12400
	v_mov_b32_e32 v113, 0x4b400000
	v_mov_b32_e32 v114, 0x4b400008
	v_mov_b32_e32 v115, 0x4b400010
	v_add_u32_e32 v116, 0x1c5a0, v93
	v_add_u32_e32 v117, 0x1c400, v93
	v_mbcnt_lo_u32_b32 v200, -1, 0
	v_mbcnt_hi_u32_b32 v200, -1, v200
	v_and_b32_e32 v201, 3, v200
	v_and_b32_e32 v202, 15, v200
	v_cmp_gt_u32_e32 vcc, 8, v202
	s_nop 1
	v_cndmask_b32_e64 v178, 0, v112, vcc
	v_cndmask_b32_e64 v179, v112, 0, vcc
	v_lshlrev_b32_e32 v181, 1, v201
	v_sub_u32_e32 v202, 22, v181
	v_lshlrev_b32_e64 v180, v202, 1
	v_sub_u32_e32 v202, 16, v181
	v_lshlrev_b32_e64 v181, v202, 1
	v_readfirstlane_b32 s51, v117
	v_lshrrev_b32_e32 v202, 4, v200
	v_lshlrev_b32_e32 v192, 5, v202
	v_bfe_u32 v202, v200, 2, 1
	v_mul_u32_u24_e32 v202, 0x110, v202
	v_add_u32_e32 v192, v192, v202
	v_add_u32_e32 v192, 0x1c400, v192
	s_sub_u32 s51, s51, 0x1c400
	s_mul_i32 s46, s51, 0xaaab
	s_lshr_b32 s46, s46, 15
	v_bfe_u32 v202, v200, 4, 1
	v_mul_u32_u24_e32 v184, 0x110, v202
	v_lshrrev_b32_e32 v202, 5, v200
	v_mul_u32_u24_e32 v202, 12, v202
	v_add_u32_e32 v184, v184, v202
	v_bfe_u32 v202, v200, 2, 2
	v_mul_u32_u24_e32 v164, 3, v202
	v_add3_u32 v184, v184, v164, v201
	v_add_u32_e32 v184, s46, v184
	v_add_u32_e32 v202, 0x1c500, v202
	v_lshrrev_b32_e32 v164, 4, v200
	v_and_b32_e32 v165, 1, v164
	v_mul_u32_u24_e32 v165, 0x110, v165
	v_lshrrev_b32_e32 v164, 1, v164
	v_lshl_add_u32 v165, v164, 2, v165
	v_add_u32_e32 v202, v202, v165
	v_add_u32_e32 v184, 0x1c400, v184
	v_cmp_eq_u32_e32 vcc, 3, v201
	s_nop 1
	v_cndmask_b32_e32 v184, v184, v202, vcc
	v_subrev_u32_e32 v185, s12, v0
	s_movk_i32 s44, 0x780
	s_movk_i32 s45, 0x800
	s_lshr_b32 s46, s44, 3
	s_add_i32 s46, s46, 1
	s_mul_i32 s46, s46, 0x6000
	s_mov_b32 s47, 0
	v_lshl_add_u64 v[196:197], v[98:99], 0, s[46:47]
	s_mov_b32 s42, 0x6000
	s_mov_b32 s43, 0
	s_sub_i32 s46, s44, 1
	s_sub_i32 s47, 0x800, s44
	s_and_b64 s[40:41], s[20:21], exec
	s_cselect_b32 s46, s46, s47
	s_cselect_b32 s41, 0, -1
	s_xor_b32 s40, s41, 0x400
	s_sub_i32 s40, s40, s41
	s_ashr_i32 s47, s46, 31
	s_lshl_b64 s[46:47], s[46:47], 10
	s_add_u32 s48, s12, s46
	s_addc_u32 s49, s13, s47
	s_waitcnt vmcnt(0) lgkmcnt(0)
	v_mov_b32_e32 v176, v118
	v_add_f32_e32 v169, -1.0, v118
	v_rcp_f32_e32 v186, v102
	s_nop 1
	v_mul_f32_e32 v188, v103, v186
	v_mov_b32_e32 v189, 0
	v_mov_b32_e32 v190, 0
	v_mov_b32_e32 v191, 0
	s_nop 1
	s_cmp_lt_i32 s44, s45
	s_cbranch_scc0 .Lscan_exit_f2
	ds_read_b128 v[122:125], v192
	ds_read_b64 v[126:127], v192 offset:16
	s_waitcnt lgkmcnt(0)
	s_cmp_lt_u32 s51, 96
	s_cbranch_scc0 .Lscan_entry_b_f2
	s_branch .Lscan_enter_a_f2
	.p2align 8
